# output row stores written through (sc1) instead of nt
# speedup vs baseline: 1.0044x; 1.0024x over previous
.LBB1_8:
	s_or_b64 exec, exec, s[2:3]
	v_lshl_or_b32 v2, v97, 6, v89
	v_ashrrev_i32_e32 v3, 31, v2
	s_add_i32 s2, s51, 1
	v_cmp_eq_u32_e32 vcc, s51, v84
	v_lshl_add_u64 v[2:3], v[2:3], 3, s[26:27]
	v_add_u32_e32 v90, s39, v90
	v_add_u32_e32 v91, s48, v91
	s_or_b64 s[36:37], vcc, s[36:37]
	s_mov_b32 s51, s2
	global_store_dwordx2 v[2:3], v[0:1], off sc1
	s_andn2_b64 exec, exec, s[36:37]
	s_cbranch_execz .LBB1_216
